# P5/P6 selection waves at s_setprio 1, weight-streaming waves at 0
# speedup vs baseline: 1.0071x; 1.0071x over previous
.LBB0_518:
	s_setprio 1
	s_add_u32 s3, s44, 0x70098000
	s_addc_u32 s26, s45, 0
	s_lshl_b32 s4, s52, 10
	s_add_i32 s27, s4, 0
	s_waitcnt vmcnt(32)
	v_mov_b32_e32 v5, 0
	v_lshlrev_b32_e32 v4, 3, v194
	s_mul_i32 s4, s52, 0x3d00
	v_lshl_add_u64 v[2:3], s[44:45], 0, v[4:5]
	v_add_u32_e32 v9, s27, v4
	v_mbcnt_lo_u32_b32 v4, -1, 0
	s_add_i32 s28, s27, s4
	v_lshlrev_b32_e32 v1, 2, v194
	s_mov_b64 s[6:7], 0x98a98000
	v_mbcnt_hi_u32_b32 v12, -1, v4
	v_mov_b32_e32 v4, -1
	v_cmp_eq_u32_e64 s[4:5], 0, v194
	v_add_u32_e32 v8, s28, v1
	v_lshl_add_u64 v[2:3], v[2:3], 0, s[6:7]
	v_or_b32_e32 v10, 64, v194
	s_add_i32 s29, 0, 0x23fc0
	s_movk_i32 s30, 0xff
	v_lshlrev_b32_e32 v11, 1, v194
	s_movk_i32 s31, 0x7ff
	s_movk_i32 s34, 0x17ff
	s_brev_b32 s35, 1
	s_movk_i32 s36, 0x1ff
	s_movk_i32 s37, 0x2ff
	s_movk_i32 s38, 0x4ff
	s_movk_i32 s39, 0x5ff
	s_movk_i32 s40, 0x6ff
	s_movk_i32 s41, 0x8ff
	s_movk_i32 s42, 0x9ff
	s_movk_i32 s43, 0xaff
	s_movk_i32 s49, 0xcff
	s_movk_i32 s53, 0xdff
	s_movk_i32 s54, 0xeff
	s_movk_i32 s55, 0xfff
	s_movk_i32 s56, 0x10ff
	s_movk_i32 s57, 0x11ff
	s_movk_i32 s58, 0x12ff
	s_movk_i32 s59, 0x14ff
	s_movk_i32 s60, 0x15ff
	s_movk_i32 s61, 0x16ff
	s_movk_i32 s62, 0x100
	s_movk_i32 s63, 0x4000
	s_movk_i32 s64, 0x3ff
	s_movk_i32 s65, 0xbff
	s_movk_i32 s67, 0x13ff
	v_mov_b32_e32 v13, 0x100
	v_mov_b32_e32 v5, v4
	s_branch .LBB0_522

.LBB0_1665:
	s_setprio 0
	s_cmp_gt_i32 s47, 7
	s_cselect_b64 s[4:5], -1, 0
	s_and_b64 s[6:7], s[54:55], s[4:5]
	s_andn2_b64 vcc, exec, s[6:7]
	s_cbranch_vccnz .LBB0_1715
	s_waitcnt vmcnt(0)
	v_cmp_eq_u32_e32 vcc, 0, v0
	s_waitcnt vmcnt(0) lgkmcnt(0)
	s_barrier
	s_and_saveexec_b64 s[6:7], vcc
	s_cbranch_execz .LBB0_1714
	s_add_i32 s3, 0, 0x23ff0
	v_mov_b32_e32 v1, s3
	s_waitcnt vmcnt(0) expcnt(0) lgkmcnt(0)
	ds_read_b32 v3, v1
	s_add_i32 s3, 0, 0x23ff4
	v_mov_b32_e32 v1, s3
	ds_read_b32 v1, v1
	s_waitcnt lgkmcnt(1)
	v_cmp_ne_u32_e32 vcc, 0, v3
	s_cbranch_vccnz .LBB0_1682
	s_load_dwordx2 s[12:13], s[50:51], 0x4
	s_add_u32 s8, s44, 0x1000
	s_addc_u32 s9, s45, 0
	s_add_u32 s10, s44, 0x1100
	s_addc_u32 s11, s45, 0
	s_waitcnt lgkmcnt(0)
	s_mul_i32 s3, s12, s48
	s_add_u32 s12, s44, 0x1200
	s_mul_i32 s3, s3, s13
	s_addc_u32 s13, s45, 0
	s_add_u32 s14, s44, 0x1300
	s_addc_u32 s15, s45, 0
	s_mov_b32 s22, 1
	v_mov_b32_e32 v17, 0
	s_branch .LBB0_1670
